# GDN chunk-local step 1: K^T/V^T LDS staging with packed dword writes (lane pairs exchange via DPP + v_perm) instead of 64 16-bit LDS writes per thread
# baseline (speedup 1.0000x reference)
.LBB0_1467:
	v_mov_b32_e32 v61, v3
	v_mov_b32_e32 v0, v68
	s_waitcnt vmcnt(0)
	v_and_b32_e32 v210, 63, v68
	v_lshrrev_b32_e32 v211, 6, v68
	v_and_b32_e32 v206, 1, v210
	v_and_b32_e32 v212, 62, v210
	v_mul_u32_u24_e32 v211, 0x480, v211
	v_mul_u32_u24_e32 v213, 0x90, v206
	v_sub_u32_e32 v214, 62, v212
	v_add3_u32 v211, v3, v211, v213
	v_cmp_eq_u32_e32 vcc, 0, v206
	v_lshl_add_u32 v202, v212, 1, v211
	v_lshl_add_u32 v203, v214, 1, v211
	v_mov_b32_e32 v212, 0x03020706
	v_mov_b32_e32 v213, 0x05040100
	v_mov_b32_e32 v214, 0x07060302
	v_mov_b32_e32 v215, 0x01000504
	v_cndmask_b32_e32 v200, v212, v213, vcc
	v_cndmask_b32_e32 v201, v214, v215, vcc
	v_add_u32_e32 v204, 0x12000, v202
	v_add_u32_e32 v205, 0x12000, v203
	v_mov_b32_dpp v207, v36 quad_perm:[1,0,3,2] row_mask:0xf bank_mask:0xf
	v_perm_b32 v208, v207, v36, v200
	v_perm_b32 v209, v207, v36, v201
	ds_write_b32 v202, v208 offset:36864
	ds_write_b32 v203, v209 offset:55296
	v_mov_b32_dpp v207, v44 quad_perm:[1,0,3,2] row_mask:0xf bank_mask:0xf
	v_perm_b32 v208, v207, v44, v200
	v_perm_b32 v209, v207, v44, v201
	ds_write_b32 v204, v208 offset:0
	ds_write_b32 v205, v209 offset:18432
	v_mov_b32_dpp v207, v37 quad_perm:[1,0,3,2] row_mask:0xf bank_mask:0xf
	v_perm_b32 v208, v207, v37, v200
	v_perm_b32 v209, v207, v37, v201
	ds_write_b32 v202, v208 offset:37152
	ds_write_b32 v203, v209 offset:55584
	v_mov_b32_dpp v207, v45 quad_perm:[1,0,3,2] row_mask:0xf bank_mask:0xf
	v_perm_b32 v208, v207, v45, v200
	v_perm_b32 v209, v207, v45, v201
	ds_write_b32 v204, v208 offset:288
	ds_write_b32 v205, v209 offset:18720
	v_mov_b32_dpp v207, v38 quad_perm:[1,0,3,2] row_mask:0xf bank_mask:0xf
	v_perm_b32 v208, v207, v38, v200
	v_perm_b32 v209, v207, v38, v201
	ds_write_b32 v202, v208 offset:37440
	ds_write_b32 v203, v209 offset:55872
	v_mov_b32_dpp v207, v46 quad_perm:[1,0,3,2] row_mask:0xf bank_mask:0xf
	v_perm_b32 v208, v207, v46, v200
	v_perm_b32 v209, v207, v46, v201
	ds_write_b32 v204, v208 offset:576
	ds_write_b32 v205, v209 offset:19008
	v_mov_b32_dpp v207, v39 quad_perm:[1,0,3,2] row_mask:0xf bank_mask:0xf
	v_perm_b32 v208, v207, v39, v200
	v_perm_b32 v209, v207, v39, v201
	ds_write_b32 v202, v208 offset:37728
	ds_write_b32 v203, v209 offset:56160
	v_mov_b32_dpp v207, v47 quad_perm:[1,0,3,2] row_mask:0xf bank_mask:0xf
	v_perm_b32 v208, v207, v47, v200
	v_perm_b32 v209, v207, v47, v201
	ds_write_b32 v204, v208 offset:864
	ds_write_b32 v205, v209 offset:19296
	v_mov_b32_dpp v207, v52 quad_perm:[1,0,3,2] row_mask:0xf bank_mask:0xf
	v_perm_b32 v208, v207, v52, v200
	v_perm_b32 v209, v207, v52, v201
	ds_write_b32 v202, v208 offset:46080
	ds_write_b32 v203, v209 offset:64512
	v_mov_b32_dpp v207, v56 quad_perm:[1,0,3,2] row_mask:0xf bank_mask:0xf
	v_perm_b32 v208, v207, v56, v200
	v_perm_b32 v209, v207, v56, v201
	ds_write_b32 v204, v208 offset:9216
	ds_write_b32 v205, v209 offset:27648
	v_mov_b32_dpp v207, v53 quad_perm:[1,0,3,2] row_mask:0xf bank_mask:0xf
	v_perm_b32 v208, v207, v53, v200
	v_perm_b32 v209, v207, v53, v201
	ds_write_b32 v202, v208 offset:46368
	ds_write_b32 v203, v209 offset:64800
	v_mov_b32_dpp v207, v57 quad_perm:[1,0,3,2] row_mask:0xf bank_mask:0xf
	v_perm_b32 v208, v207, v57, v200
	v_perm_b32 v209, v207, v57, v201
	ds_write_b32 v204, v208 offset:9504
	ds_write_b32 v205, v209 offset:27936
	v_mov_b32_dpp v207, v54 quad_perm:[1,0,3,2] row_mask:0xf bank_mask:0xf
	v_perm_b32 v208, v207, v54, v200
	v_perm_b32 v209, v207, v54, v201
	ds_write_b32 v202, v208 offset:46656
	ds_write_b32 v203, v209 offset:65088
	v_mov_b32_dpp v207, v58 quad_perm:[1,0,3,2] row_mask:0xf bank_mask:0xf
	v_perm_b32 v208, v207, v58, v200
	v_perm_b32 v209, v207, v58, v201
	ds_write_b32 v204, v208 offset:9792
	ds_write_b32 v205, v209 offset:28224
	v_mov_b32_dpp v207, v55 quad_perm:[1,0,3,2] row_mask:0xf bank_mask:0xf
	v_perm_b32 v208, v207, v55, v200
	v_perm_b32 v209, v207, v55, v201
	ds_write_b32 v202, v208 offset:46944
	ds_write_b32 v203, v209 offset:65376
	v_mov_b32_dpp v207, v59 quad_perm:[1,0,3,2] row_mask:0xf bank_mask:0xf
	v_perm_b32 v208, v207, v59, v200
	v_perm_b32 v209, v207, v59, v201
	ds_write_b32 v204, v208 offset:10080
	ds_write_b32 v205, v209 offset:28512
	v_lshrrev_b32_e32 v9, 16, v36
	v_and_b32_e32 v21, 63, v0
	v_mul_u32_u24_e32 v1, 0x88, v21
	v_ashrrev_i32_e32 v60, 3, v0
	v_lshl_add_u32 v1, v1, 1, v61
	v_and_b32_e32 v4, -8, v60
	v_lshl_add_u32 v6, v4, 1, v1
	v_bitop3_b32 v27, v0, 63, v0 bitop3:0xc
	ds_write_b128 v6, v[40:43] offset:18432
	ds_write_b128 v6, v[36:39]
	v_mul_lo_u32 v6, v4, s33
	v_add_u32_e32 v5, 0x16800, v61
	v_add_u32_e32 v7, v61, v6
	v_lshlrev_b32_e32 v11, 1, v21
	v_lshlrev_b32_e32 v13, 1, v27
	v_add_u32_e32 v2, 0x12000, v61
	v_add_u32_e32 v8, v5, v6
	v_add_u32_e32 v12, v7, v11
	v_add_u32_e32 v14, v7, v13
	v_sub_u32_e32 v7, v7, v11
	v_lshrrev_b32_e32 v10, 16, v44
	v_add3_u32 v6, v2, v6, v11
	v_add_u32_e32 v9, v8, v13
	v_sub_u32_e32 v8, v8, v11
	v_lshrrev_b32_e32 v9, 16, v37
	v_lshrrev_b32_e32 v10, 16, v45
	v_add_u32_e32 v33, 0x200, v0
	v_lshrrev_b32_e32 v9, 16, v38
	v_lshrrev_b32_e32 v10, 16, v46
	v_ashrrev_i32_e32 v71, 3, v33
	v_lshrrev_b32_e32 v9, 16, v39
	v_lshrrev_b32_e32 v10, 16, v47
	v_and_b32_e32 v6, -8, v71
	v_lshl_add_u32 v1, v6, 1, v1
	ds_write_b128 v1, v[48:51] offset:18432
	ds_write_b128 v1, v[52:55]
	v_mul_lo_u32 v1, v6, s33
	v_ashrrev_i32_e32 v26, 6, v0
	v_add_u32_e32 v7, v61, v1
	v_add_u32_e32 v5, v5, v1
	v_lshrrev_b32_e32 v8, 16, v52
	v_add_u32_e32 v10, v7, v11
	v_add_u32_e32 v12, v7, v13
	v_sub_u32_e32 v7, v7, v11
	v_add3_u32 v1, v2, v1, v11
	v_add_u32_e32 v2, v5, v13
	v_readfirstlane_b32 s10, v26
	v_lshrrev_b32_e32 v9, 16, v56
	v_sub_u32_e32 v2, v5, v11
	v_lshrrev_b32_e32 v5, 16, v53
	v_lshrrev_b32_e32 v8, 16, v57
	s_cmp_lt_i32 s10, 2
	v_lshlrev_b32_e32 v28, 2, v21
	v_add_u32_e32 v22, 0x23400, v61
	v_lshrrev_b32_e32 v5, 16, v54
	v_lshrrev_b32_e32 v8, 16, v58
	v_add_u32_e32 v23, 0x23200, v61
	s_cselect_b64 s[2:3], -1, 0
	s_cmp_gt_i32 s10, 1
	v_cmp_eq_u32_e32 vcc, 0, v21
	v_lshl_or_b32 v24, s10, 8, v28
	v_lshrrev_b32_e32 v5, 16, v55
	v_lshrrev_b32_e32 v8, 16, v59
	s_cbranch_scc1 .LBB0_1469
	v_add_u32_e32 v1, -4, v28
	ds_bpermute_b32 v1, v1, v69
	v_add_u32_e32 v2, -8, v28
	s_waitcnt lgkmcnt(0)
	v_add_f32_e32 v1, v69, v1
	v_cndmask_b32_e32 v1, v1, v69, vcc
	ds_bpermute_b32 v2, v2, v1
	v_cmp_gt_u32_e32 vcc, 2, v21
	s_waitcnt lgkmcnt(0)
	v_add_f32_e32 v2, v1, v2
	v_cndmask_b32_e32 v1, v2, v1, vcc
	v_add_u32_e32 v2, -16, v28
	ds_bpermute_b32 v2, v2, v1
	v_cmp_gt_u32_e32 vcc, 4, v21
	s_waitcnt lgkmcnt(0)
	v_add_f32_e32 v2, v1, v2
	v_cndmask_b32_e32 v1, v2, v1, vcc
	v_subrev_u32_e32 v2, 32, v28
	ds_bpermute_b32 v2, v2, v1
	v_cmp_gt_u32_e32 vcc, 8, v21
	s_waitcnt lgkmcnt(0)
	v_add_f32_e32 v2, v1, v2
	v_cndmask_b32_e32 v1, v2, v1, vcc
	v_subrev_u32_e32 v2, 64, v28
	ds_bpermute_b32 v2, v2, v1
	v_cmp_gt_u32_e32 vcc, 16, v21
	s_waitcnt lgkmcnt(0)
	v_add_f32_e32 v2, v1, v2
	v_cndmask_b32_e32 v1, v2, v1, vcc
	v_add_u32_e32 v2, 0xffffff80, v28
	ds_bpermute_b32 v2, v2, v1
	v_cmp_gt_u32_e32 vcc, 32, v21
	s_waitcnt lgkmcnt(0)
	v_add_f32_e32 v2, v1, v2
	v_cndmask_b32_e32 v1, v2, v1, vcc
	v_add_u32_e32 v2, v23, v24
	ds_write_b32 v2, v1
	v_add_u32_e32 v1, v22, v24
	ds_write_b32 v1, v70
